# grid/XCC barrier: the consumer CU's L1 invalidate (buffer_inv sc1) issued at the workgroup's arrival, overlapped with the wait, instead of after the release is observed
# speedup vs baseline: 1.0135x; 1.0135x over previous
; __device__ __forceinline__ void xcd_barrier_complete(unsigned* bar, unsigned x, unsigned& nloc, unsigned& nx, unsigned& bal) {
;     const unsigned G = gridDim.x * gridDim.y * gridDim.z;
;     unsigned sum, cnt, mine, even, sp = 0u;
;     for (;;) {
;         sum = 0u; cnt = 0u; mine = 0u; even = 1u;
; __device__ __forceinline__ void xcd_barrier(const XcdBarrier& b, const bool xb_leader) {
;     asm volatile("s_waitcnt vmcnt(0)" ::: "memory");
;     __syncthreads();
;     if (xb_leader) {
;         unsigned* bar = b.bar;
;         __builtin_amdgcn_s_waitcnt(0);
;         unsigned nloc = b.st[0], nx = b.st[1];
;         if (nloc == 0u) { unsigned bal; xcd_barrier_complete(bar, b.x, nloc, nx, bal); b.st[0] = nloc; b.st[1] = nx; b.st[3] = bal; }
.LBB0_62:
	s_waitcnt vmcnt(0)
	s_waitcnt lgkmcnt(0)
	s_barrier
	s_and_saveexec_b64 s[10:11], s[4:5]
	s_cbranch_execz .LBB0_121
	s_add_i32 s3, 0, 0x20160
	v_mov_b32_e32 v0, s3
	s_waitcnt vmcnt(0) expcnt(0) lgkmcnt(0)
	buffer_inv sc1
	ds_read_b32 v9, v0
	s_add_i32 s3, 0, 0x20164
	v_mov_b32_e32 v0, s3
	ds_read_b32 v8, v0
	s_waitcnt lgkmcnt(1)
	v_cmp_ne_u32_e32 vcc, 0, v9
	s_cbranch_vccnz .LBB0_85
	v_readlane_b32 s4, v254, 0
	v_readlane_b32 s5, v254, 1
	s_load_dwordx2 s[12:13], s[4:5], 0x4
	s_add_u32 s4, s28, 0x1000
	s_addc_u32 s5, s29, 0
	s_add_u32 s6, s28, 0x1100
	s_addc_u32 s7, s29, 0
	s_waitcnt lgkmcnt(0)
	s_mul_i32 s3, s12, s33
	s_add_u32 s12, s28, 0x1200
	s_mul_i32 s3, s3, s13
	s_addc_u32 s13, s29, 0
	s_add_u32 s14, s28, 0x1300
	s_addc_u32 s15, s29, 0
	s_mov_b32 s36, 1
	v_mov_b32_e32 v8, 0
	s_branch .LBB0_67

; __device__ __forceinline__ unsigned xb_ld(unsigned* p)              { return __hip_atomic_load(p, __ATOMIC_RELAXED, __HIP_MEMORY_SCOPE_AGENT); }
; #define XB_SPIN(cond, bar) do { unsigned _sp = 0; while (cond) { __builtin_amdgcn_s_sleep(1); \
;     if ((++_sp & 255u) == 0u) { if (xb_ld(&(bar)[XB_TMO])) break; if (_sp > XB_SPIN_CAP) { atomicAdd(&(bar)[XB_TMO], 1u); break; } } } } while (0)
; __device__ __forceinline__ void xcd_barrier(const XcdBarrier& b, const bool xb_leader) {
;     ...
;             XB_SPIN(xb_ld(&bar[XB_XGEN(b.x)]) == gen, bar);
;             __builtin_amdgcn_fence(__ATOMIC_ACQUIRE, "agent");
;             asm volatile("s_waitcnt vmcnt(0)" ::: "memory");
.LBB0_100:
	s_or_b64 exec, exec, s[12:13]
	s_waitcnt vmcnt(0) lgkmcnt(0)
	s_waitcnt vmcnt(0)

; __device__ __forceinline__ unsigned xb_ld(unsigned* p)              { return __hip_atomic_load(p, __ATOMIC_RELAXED, __HIP_MEMORY_SCOPE_AGENT); }
; __device__ __forceinline__ unsigned xb_add(unsigned* p, unsigned v) { return __hip_atomic_fetch_add(p, v, __ATOMIC_RELAXED, __HIP_MEMORY_SCOPE_AGENT); }
; #define XB_SPIN(cond, bar) do { unsigned _sp = 0; while (cond) { __builtin_amdgcn_s_sleep(1); \
;     if ((++_sp & 255u) == 0u) { if (xb_ld(&(bar)[XB_TMO])) break; if (_sp > XB_SPIN_CAP) { atomicAdd(&(bar)[XB_TMO], 1u); break; } } } } while (0)
; __device__ __forceinline__ void xcd_barrier(const XcdBarrier& b, const bool xb_leader) {
;     ...
;             else XB_SPIN(xb_ld(&bar[XB_TOPGEN]) == tg, bar);
;             __builtin_amdgcn_fence(__ATOMIC_ACQUIRE, "agent");
;             xb_add(&bar[XB_XGEN(b.x)], 1u);
;             asm volatile("s_waitcnt vmcnt(0)" ::: "memory");
.LBB0_118:
	s_or_b64 exec, exec, s[6:7]
	s_mov_b64 s[6:7], exec
	v_mbcnt_lo_u32_b32 v0, s6, 0
	v_mbcnt_hi_u32_b32 v0, s7, v0
	v_cmp_eq_u32_e32 vcc, 0, v0
	s_waitcnt vmcnt(0)
	s_and_saveexec_b64 s[12:13], vcc
	s_cbranch_execz .LBB0_120
	s_bcnt1_i32_b64 s3, s[6:7]
	v_mov_b32_e32 v0, 0x2000
	v_mov_b32_e32 v1, s3
	global_atomic_add v0, v1, s[4:5] offset:1024

; __device__ __forceinline__ unsigned xb_ld(unsigned* p)              { return __hip_atomic_load(p, __ATOMIC_RELAXED, __HIP_MEMORY_SCOPE_AGENT); }
; __device__ __forceinline__ unsigned xb_add(unsigned* p, unsigned v) { return __hip_atomic_fetch_add(p, v, __ATOMIC_RELAXED, __HIP_MEMORY_SCOPE_AGENT); }
; #define XB_SPIN(cond, bar) do { unsigned _sp = 0; while (cond) { __builtin_amdgcn_s_sleep(1); \
;     if ((++_sp & 255u) == 0u) { if (xb_ld(&(bar)[XB_TMO])) break; if (_sp > XB_SPIN_CAP) { atomicAdd(&(bar)[XB_TMO], 1u); break; } } } } while (0)
; __device__ __forceinline__ void xcc_barrier(unsigned* bar, unsigned* cnt, unsigned nloc, const bool xb_leader) {
;     asm volatile("s_waitcnt vmcnt(0)" ::: "memory");
;     __syncthreads();
;     if (xb_leader) {
;         __builtin_amdgcn_s_waitcnt(0);
;         const unsigned old = xb_add(cnt, 1u), target = (old / nloc + 1u) * nloc;
;         XB_SPIN(xb_ld(cnt) < target, bar);
.LBB0_134:
	s_waitcnt vmcnt(0)
	s_waitcnt lgkmcnt(0)
	s_barrier
	s_and_saveexec_b64 s[4:5], s[6:7]
	s_cbranch_execz .LBB0_150
	s_lshl_b32 s6, s82, 10
	s_ashr_i32 s7, s6, 31
	s_lshl_b64 s[6:7], s[6:7], 2
	s_add_u32 s3, s78, s6
	s_addc_u32 s6, s79, s7
	v_readlane_b32 s7, v254, 21
	s_lshl_b32 s7, s7, 8
	s_mov_b64 s[8:9], exec
	s_add_u32 s3, s3, s7
	s_addc_u32 s7, s6, 0
	v_mbcnt_lo_u32_b32 v0, s8, 0
	s_add_u32 s6, s3, 0xc000
	v_mbcnt_hi_u32_b32 v1, s9, v0
	s_addc_u32 s7, s7, 0
	v_cmp_eq_u32_e32 vcc, 0, v1
	s_waitcnt vmcnt(0) expcnt(0) lgkmcnt(0)
	buffer_inv sc1
	s_and_saveexec_b64 s[10:11], vcc
	s_cbranch_execz .LBB0_137
	s_bcnt1_i32_b64 s3, s[8:9]
	v_mov_b32_e32 v0, 0
	v_mov_b32_e32 v2, s3
	global_atomic_add v2, v0, v2, s[6:7] sc0

; __device__ __forceinline__ unsigned xb_ld(unsigned* p)              { return __hip_atomic_load(p, __ATOMIC_RELAXED, __HIP_MEMORY_SCOPE_AGENT); }
; #define XB_SPIN(cond, bar) do { unsigned _sp = 0; while (cond) { __builtin_amdgcn_s_sleep(1); \
;     if ((++_sp & 255u) == 0u) { if (xb_ld(&(bar)[XB_TMO])) break; if (_sp > XB_SPIN_CAP) { atomicAdd(&(bar)[XB_TMO], 1u); break; } } } } while (0)
; __device__ __forceinline__ void xcc_barrier(unsigned* bar, unsigned* cnt, unsigned nloc, const bool xb_leader) {
;     ...
;         XB_SPIN(xb_ld(cnt) < target, bar);
;         __builtin_amdgcn_fence(__ATOMIC_ACQUIRE, "agent");
;         asm volatile("s_waitcnt vmcnt(0)" ::: "memory");
.LBB0_149:
	s_or_b64 exec, exec, s[8:9]
	s_waitcnt vmcnt(0)
	s_waitcnt vmcnt(0)

; __device__ __forceinline__ void xcd_barrier(const XcdBarrier& b, const bool xb_leader) {
;     asm volatile("s_waitcnt vmcnt(0)" ::: "memory");
;     __syncthreads();
;     if (xb_leader) {
;         unsigned* bar = b.bar;
;         __builtin_amdgcn_s_waitcnt(0);
;         unsigned nloc = b.st[0], nx = b.st[1];
;         if (nloc == 0u) { unsigned bal; xcd_barrier_complete(bar, b.x, nloc, nx, bal); b.st[0] = nloc; b.st[1] = nx; b.st[3] = bal; }
.LBB0_154:
	s_waitcnt vmcnt(0)
	s_waitcnt lgkmcnt(0)
	s_barrier
	s_and_saveexec_b64 s[4:5], s[6:7]
	s_cbranch_execz .LBB0_214
	s_add_i32 s3, 0, 0x20160
	v_mov_b32_e32 v0, s3
	s_waitcnt vmcnt(0) expcnt(0) lgkmcnt(0)
	buffer_inv sc1
	ds_read_b32 v9, v0
	s_add_i32 s3, 0, 0x20164
	v_mov_b32_e32 v0, s3
	ds_read_b32 v8, v0
	s_waitcnt lgkmcnt(1)
	v_cmp_ne_u32_e32 vcc, 0, v9
	s_cbranch_vccnz .LBB0_178
	v_readlane_b32 s6, v254, 0
	v_readlane_b32 s7, v254, 1
	s_load_dwordx2 s[10:11], s[6:7], 0x4
	s_add_u32 s6, s28, 0x1000
	s_addc_u32 s7, s29, 0
	s_add_u32 s8, s28, 0x1100
	s_addc_u32 s9, s29, 0
	s_waitcnt lgkmcnt(0)
	s_mul_i32 s3, s10, s33
	s_add_u32 s10, s28, 0x1200
	s_mul_i32 s3, s3, s11
	s_addc_u32 s11, s29, 0
	s_add_u32 s12, s28, 0x1300
	s_addc_u32 s13, s29, 0
	s_mov_b32 s36, 1
	v_mov_b32_e32 v8, 0
	s_branch .LBB0_159

; __device__ __forceinline__ unsigned xb_ld(unsigned* p)              { return __hip_atomic_load(p, __ATOMIC_RELAXED, __HIP_MEMORY_SCOPE_AGENT); }
; #define XB_SPIN(cond, bar) do { unsigned _sp = 0; while (cond) { __builtin_amdgcn_s_sleep(1); \
;     if ((++_sp & 255u) == 0u) { if (xb_ld(&(bar)[XB_TMO])) break; if (_sp > XB_SPIN_CAP) { atomicAdd(&(bar)[XB_TMO], 1u); break; } } } } while (0)
; __device__ __forceinline__ void xcd_barrier(const XcdBarrier& b, const bool xb_leader) {
;     ...
;             XB_SPIN(xb_ld(&bar[XB_XGEN(b.x)]) == gen, bar);
;             __builtin_amdgcn_fence(__ATOMIC_ACQUIRE, "agent");
;             asm volatile("s_waitcnt vmcnt(0)" ::: "memory");
.LBB0_193:
	s_or_b64 exec, exec, s[10:11]
	s_waitcnt vmcnt(0) lgkmcnt(0)
	s_waitcnt vmcnt(0)

; __device__ __forceinline__ unsigned xb_ld(unsigned* p)              { return __hip_atomic_load(p, __ATOMIC_RELAXED, __HIP_MEMORY_SCOPE_AGENT); }
; __device__ __forceinline__ unsigned xb_add(unsigned* p, unsigned v) { return __hip_atomic_fetch_add(p, v, __ATOMIC_RELAXED, __HIP_MEMORY_SCOPE_AGENT); }
; #define XB_SPIN(cond, bar) do { unsigned _sp = 0; while (cond) { __builtin_amdgcn_s_sleep(1); \
;     if ((++_sp & 255u) == 0u) { if (xb_ld(&(bar)[XB_TMO])) break; if (_sp > XB_SPIN_CAP) { atomicAdd(&(bar)[XB_TMO], 1u); break; } } } } while (0)
; __device__ __forceinline__ void xcd_barrier(const XcdBarrier& b, const bool xb_leader) {
;     ...
;             else XB_SPIN(xb_ld(&bar[XB_TOPGEN]) == tg, bar);
;             __builtin_amdgcn_fence(__ATOMIC_ACQUIRE, "agent");
;             xb_add(&bar[XB_XGEN(b.x)], 1u);
;             asm volatile("s_waitcnt vmcnt(0)" ::: "memory");
.LBB0_211:
	s_or_b64 exec, exec, s[8:9]
	s_mov_b64 s[8:9], exec
	v_mbcnt_lo_u32_b32 v0, s8, 0
	v_mbcnt_hi_u32_b32 v0, s9, v0
	v_cmp_eq_u32_e32 vcc, 0, v0
	s_waitcnt vmcnt(0)
	s_and_saveexec_b64 s[10:11], vcc
	s_cbranch_execz .LBB0_213
	s_bcnt1_i32_b64 s3, s[8:9]
	v_mov_b32_e32 v0, 0x2000
	v_mov_b32_e32 v1, s3
	global_atomic_add v0, v1, s[6:7] offset:1024

; __device__ __forceinline__ void xcd_barrier(const XcdBarrier& b, const bool xb_leader) {
;     asm volatile("s_waitcnt vmcnt(0)" ::: "memory");
;     __syncthreads();
;     if (xb_leader) {
;         unsigned* bar = b.bar;
;         __builtin_amdgcn_s_waitcnt(0);
;         unsigned nloc = b.st[0], nx = b.st[1];
;         if (nloc == 0u) { unsigned bal; xcd_barrier_complete(bar, b.x, nloc, nx, bal); b.st[0] = nloc; b.st[1] = nx; b.st[3] = bal; }
.LBB0_311:
	s_waitcnt vmcnt(0)
	s_waitcnt vmcnt(0) lgkmcnt(0)
	s_barrier
	s_and_saveexec_b64 s[0:1], s[6:7]
	s_cbranch_execz .LBB0_370
	s_add_i32 s3, 0, 0x20160
	v_mov_b32_e32 v0, s3
	s_waitcnt vmcnt(0) expcnt(0) lgkmcnt(0)
	buffer_inv sc1
	ds_read_b32 v9, v0
	s_add_i32 s3, 0, 0x20164
	v_mov_b32_e32 v0, s3
	ds_read_b32 v8, v0
	s_waitcnt lgkmcnt(1)
	v_cmp_ne_u32_e32 vcc, 0, v9
	s_cbranch_vccnz .LBB0_334
	v_readlane_b32 s6, v254, 0
	v_readlane_b32 s7, v254, 1
	s_load_dwordx2 s[10:11], s[6:7], 0x4
	s_add_u32 s6, s28, 0x1000
	s_addc_u32 s7, s29, 0
	s_add_u32 s8, s28, 0x1100
	s_addc_u32 s9, s29, 0
	s_waitcnt lgkmcnt(0)
	s_mul_i32 s3, s10, s33
	s_add_u32 s10, s28, 0x1200
	s_mul_i32 s3, s3, s11
	s_addc_u32 s11, s29, 0
	s_add_u32 s12, s28, 0x1300
	s_addc_u32 s13, s29, 0
	s_mov_b32 s36, 1
	v_mov_b32_e32 v8, 0
	s_branch .LBB0_316

; __device__ __forceinline__ void xcd_barrier(const XcdBarrier& b, const bool xb_leader) {
;     asm volatile("s_waitcnt vmcnt(0)" ::: "memory");
;     __syncthreads();
;     if (xb_leader) {
;         unsigned* bar = b.bar;
;         __builtin_amdgcn_s_waitcnt(0);
;         unsigned nloc = b.st[0], nx = b.st[1];
;         if (nloc == 0u) { unsigned bal; xcd_barrier_complete(bar, b.x, nloc, nx, bal); b.st[0] = nloc; b.st[1] = nx; b.st[3] = bal; }
.LBB0_587:
	s_waitcnt vmcnt(0)
	s_waitcnt vmcnt(0) lgkmcnt(0)
	s_barrier
	s_and_saveexec_b64 s[4:5], s[6:7]
	s_cbranch_execz .LBB0_646
	s_add_i32 s3, 0, 0x20160
	v_mov_b32_e32 v0, s3
	s_waitcnt vmcnt(0) expcnt(0) lgkmcnt(0)
	buffer_inv sc1
	ds_read_b32 v9, v0
	s_add_i32 s3, 0, 0x20164
	v_mov_b32_e32 v0, s3
	ds_read_b32 v8, v0
	s_waitcnt lgkmcnt(1)
	v_cmp_ne_u32_e32 vcc, 0, v9
	s_cbranch_vccnz .LBB0_610
	v_readlane_b32 s6, v254, 0
	v_readlane_b32 s7, v254, 1
	s_load_dwordx2 s[10:11], s[6:7], 0x4
	s_add_u32 s6, s28, 0x1000
	s_addc_u32 s7, s29, 0
	s_add_u32 s8, s28, 0x1100
	s_addc_u32 s9, s29, 0
	s_waitcnt lgkmcnt(0)
	s_mul_i32 s3, s10, s33
	s_add_u32 s10, s28, 0x1200
	s_mul_i32 s3, s3, s11
	s_addc_u32 s11, s29, 0
	s_add_u32 s12, s28, 0x1300
	s_addc_u32 s13, s29, 0
	s_mov_b32 s36, 1
	v_mov_b32_e32 v8, 0
	s_branch .LBB0_592

; __device__ __forceinline__ unsigned xb_ld(unsigned* p)              { return __hip_atomic_load(p, __ATOMIC_RELAXED, __HIP_MEMORY_SCOPE_AGENT); }
; __device__ __forceinline__ unsigned xb_add(unsigned* p, unsigned v) { return __hip_atomic_fetch_add(p, v, __ATOMIC_RELAXED, __HIP_MEMORY_SCOPE_AGENT); }
; #define XB_SPIN(cond, bar) do { unsigned _sp = 0; while (cond) { __builtin_amdgcn_s_sleep(1); \
;     if ((++_sp & 255u) == 0u) { if (xb_ld(&(bar)[XB_TMO])) break; if (_sp > XB_SPIN_CAP) { atomicAdd(&(bar)[XB_TMO], 1u); break; } } } } while (0)
; __device__ __forceinline__ void xcc_barrier(unsigned* bar, unsigned* cnt, unsigned nloc, const bool xb_leader) {
;     asm volatile("s_waitcnt vmcnt(0)" ::: "memory");
;     __syncthreads();
;     if (xb_leader) {
;         __builtin_amdgcn_s_waitcnt(0);
;         const unsigned old = xb_add(cnt, 1u), target = (old / nloc + 1u) * nloc;
;         XB_SPIN(xb_ld(cnt) < target, bar);
.LBB0_745:
	s_waitcnt vmcnt(0)
	s_waitcnt vmcnt(0) lgkmcnt(0)
	s_barrier
	s_and_saveexec_b64 s[0:1], s[4:5]
	s_cbranch_execz .LBB0_791
	s_lshl_b32 s4, s82, 10
	s_ashr_i32 s5, s4, 31
	s_lshl_b64 s[4:5], s[4:5], 2
	s_add_u32 s3, s78, s4
	s_addc_u32 s4, s79, s5
	v_readlane_b32 s5, v254, 21
	s_lshl_b32 s5, s5, 8
	s_mov_b64 s[6:7], exec
	s_add_u32 s3, s3, s5
	s_addc_u32 s5, s4, 0
	v_mbcnt_lo_u32_b32 v0, s6, 0
	s_add_u32 s4, s3, 0xc000
	v_mbcnt_hi_u32_b32 v1, s7, v0
	s_addc_u32 s5, s5, 0
	v_cmp_eq_u32_e32 vcc, 0, v1
	s_waitcnt vmcnt(0) expcnt(0) lgkmcnt(0)
	buffer_inv sc1
	s_and_saveexec_b64 s[8:9], vcc
	s_cbranch_execz .LBB0_748
	s_bcnt1_i32_b64 s3, s[6:7]
	v_mov_b32_e32 v0, 0
	v_mov_b32_e32 v2, s3
	global_atomic_add v2, v0, v2, s[4:5] sc0

; __device__ __forceinline__ unsigned xb_ld(unsigned* p)              { return __hip_atomic_load(p, __ATOMIC_RELAXED, __HIP_MEMORY_SCOPE_AGENT); }
; #define XB_SPIN(cond, bar) do { unsigned _sp = 0; while (cond) { __builtin_amdgcn_s_sleep(1); \
;     if ((++_sp & 255u) == 0u) { if (xb_ld(&(bar)[XB_TMO])) break; if (_sp > XB_SPIN_CAP) { atomicAdd(&(bar)[XB_TMO], 1u); break; } } } } while (0)
; __device__ __forceinline__ void xcc_barrier(unsigned* bar, unsigned* cnt, unsigned nloc, const bool xb_leader) {
;     ...
;         XB_SPIN(xb_ld(cnt) < target, bar);
;         __builtin_amdgcn_fence(__ATOMIC_ACQUIRE, "agent");
;         asm volatile("s_waitcnt vmcnt(0)" ::: "memory");
.LBB0_790:
	s_or_b64 exec, exec, s[6:7]
	s_waitcnt vmcnt(0)
	s_waitcnt vmcnt(0)

; __device__ __forceinline__ void xcd_barrier(const XcdBarrier& b, const bool xb_leader) {
;     asm volatile("s_waitcnt vmcnt(0)" ::: "memory");
;     __syncthreads();
;     if (xb_leader) {
;         unsigned* bar = b.bar;
;         __builtin_amdgcn_s_waitcnt(0);
;         unsigned nloc = b.st[0], nx = b.st[1];
;         if (nloc == 0u) { unsigned bal; xcd_barrier_complete(bar, b.x, nloc, nx, bal); b.st[0] = nloc; b.st[1] = nx; b.st[3] = bal; }
.LBB0_795:
	s_waitcnt vmcnt(0)
	s_waitcnt vmcnt(0) lgkmcnt(0)
	s_barrier
	s_and_saveexec_b64 s[0:1], s[4:5]
	s_cbranch_execz .LBB0_855
	s_add_i32 s3, 0, 0x20160
	v_mov_b32_e32 v0, s3
	s_waitcnt vmcnt(0) expcnt(0) lgkmcnt(0)
	buffer_inv sc1
	ds_read_b32 v9, v0
	s_add_i32 s3, 0, 0x20164
	v_mov_b32_e32 v0, s3
	ds_read_b32 v8, v0
	s_waitcnt lgkmcnt(1)
	v_cmp_ne_u32_e32 vcc, 0, v9
	s_cbranch_vccnz .LBB0_819
	v_readlane_b32 s4, v254, 0
	v_readlane_b32 s5, v254, 1
	s_load_dwordx2 s[8:9], s[4:5], 0x4
	s_add_u32 s4, s28, 0x1000
	s_addc_u32 s5, s29, 0
	s_add_u32 s6, s28, 0x1100
	s_addc_u32 s7, s29, 0
	s_waitcnt lgkmcnt(0)
	s_mul_i32 s3, s8, s33
	s_add_u32 s8, s28, 0x1200
	s_mul_i32 s3, s3, s9
	s_addc_u32 s9, s29, 0
	s_add_u32 s10, s28, 0x1300
	s_addc_u32 s11, s29, 0
	s_mov_b32 s36, 1
	v_mov_b32_e32 v8, 0
	s_branch .LBB0_800

; __device__ __forceinline__ unsigned xb_ld(unsigned* p)              { return __hip_atomic_load(p, __ATOMIC_RELAXED, __HIP_MEMORY_SCOPE_AGENT); }
; #define XB_SPIN(cond, bar) do { unsigned _sp = 0; while (cond) { __builtin_amdgcn_s_sleep(1); \
;     if ((++_sp & 255u) == 0u) { if (xb_ld(&(bar)[XB_TMO])) break; if (_sp > XB_SPIN_CAP) { atomicAdd(&(bar)[XB_TMO], 1u); break; } } } } while (0)
; __device__ __forceinline__ void xcd_barrier(const XcdBarrier& b, const bool xb_leader) {
;     ...
;             XB_SPIN(xb_ld(&bar[XB_XGEN(b.x)]) == gen, bar);
;             __builtin_amdgcn_fence(__ATOMIC_ACQUIRE, "agent");
;             asm volatile("s_waitcnt vmcnt(0)" ::: "memory");
.LBB0_834:
	s_or_b64 exec, exec, s[8:9]
	s_waitcnt vmcnt(0) lgkmcnt(0)
	s_waitcnt vmcnt(0)

; __device__ __forceinline__ unsigned xb_ld(unsigned* p)              { return __hip_atomic_load(p, __ATOMIC_RELAXED, __HIP_MEMORY_SCOPE_AGENT); }
; __device__ __forceinline__ unsigned xb_add(unsigned* p, unsigned v) { return __hip_atomic_fetch_add(p, v, __ATOMIC_RELAXED, __HIP_MEMORY_SCOPE_AGENT); }
; #define XB_SPIN(cond, bar) do { unsigned _sp = 0; while (cond) { __builtin_amdgcn_s_sleep(1); \
;     if ((++_sp & 255u) == 0u) { if (xb_ld(&(bar)[XB_TMO])) break; if (_sp > XB_SPIN_CAP) { atomicAdd(&(bar)[XB_TMO], 1u); break; } } } } while (0)
; __device__ __forceinline__ void xcd_barrier(const XcdBarrier& b, const bool xb_leader) {
;     ...
;             else XB_SPIN(xb_ld(&bar[XB_TOPGEN]) == tg, bar);
;             __builtin_amdgcn_fence(__ATOMIC_ACQUIRE, "agent");
;             xb_add(&bar[XB_XGEN(b.x)], 1u);
;             asm volatile("s_waitcnt vmcnt(0)" ::: "memory");
.LBB0_852:
	s_or_b64 exec, exec, s[6:7]
	s_mov_b64 s[6:7], exec
	v_mbcnt_lo_u32_b32 v0, s6, 0
	v_mbcnt_hi_u32_b32 v0, s7, v0
	v_cmp_eq_u32_e32 vcc, 0, v0
	s_waitcnt vmcnt(0)
	s_and_saveexec_b64 s[8:9], vcc
	s_cbranch_execz .LBB0_854
	s_bcnt1_i32_b64 s3, s[6:7]
	v_mov_b32_e32 v0, 0x2000
	v_mov_b32_e32 v1, s3
	global_atomic_add v0, v1, s[4:5] offset:1024

; __device__ __forceinline__ unsigned xb_ld(unsigned* p)              { return __hip_atomic_load(p, __ATOMIC_RELAXED, __HIP_MEMORY_SCOPE_AGENT); }
; __device__ __forceinline__ unsigned xb_add(unsigned* p, unsigned v) { return __hip_atomic_fetch_add(p, v, __ATOMIC_RELAXED, __HIP_MEMORY_SCOPE_AGENT); }
; #define XB_SPIN(cond, bar) do { unsigned _sp = 0; while (cond) { __builtin_amdgcn_s_sleep(1); \
;     if ((++_sp & 255u) == 0u) { if (xb_ld(&(bar)[XB_TMO])) break; if (_sp > XB_SPIN_CAP) { atomicAdd(&(bar)[XB_TMO], 1u); break; } } } } while (0)
; __device__ __forceinline__ void xcc_barrier(unsigned* bar, unsigned* cnt, unsigned nloc, const bool xb_leader) {
;     asm volatile("s_waitcnt vmcnt(0)" ::: "memory");
;     __syncthreads();
;     if (xb_leader) {
;         __builtin_amdgcn_s_waitcnt(0);
;         const unsigned old = xb_add(cnt, 1u), target = (old / nloc + 1u) * nloc;
;         XB_SPIN(xb_ld(cnt) < target, bar);
.LBB0_878:
	s_waitcnt vmcnt(0)
	s_waitcnt vmcnt(0) lgkmcnt(0)
	s_barrier
	s_and_saveexec_b64 s[0:1], s[6:7]
	s_cbranch_execz .LBB0_894
	s_lshl_b32 s6, s82, 10
	s_ashr_i32 s7, s6, 31
	s_lshl_b64 s[6:7], s[6:7], 2
	s_add_u32 s3, s78, s6
	s_addc_u32 s6, s79, s7
	v_readlane_b32 s7, v254, 21
	s_lshl_b32 s7, s7, 8
	s_mov_b64 s[8:9], exec
	s_add_u32 s3, s3, s7
	s_addc_u32 s7, s6, 0
	v_mbcnt_lo_u32_b32 v0, s8, 0
	s_add_u32 s6, s3, 0xc000
	v_mbcnt_hi_u32_b32 v1, s9, v0
	s_addc_u32 s7, s7, 0
	v_cmp_eq_u32_e32 vcc, 0, v1
	s_waitcnt vmcnt(0) expcnt(0) lgkmcnt(0)
	buffer_inv sc1
	s_and_saveexec_b64 s[10:11], vcc
	s_cbranch_execz .LBB0_881
	s_bcnt1_i32_b64 s3, s[8:9]
	v_mov_b32_e32 v0, 0
	v_mov_b32_e32 v2, s3
	global_atomic_add v2, v0, v2, s[6:7] sc0

; __device__ __forceinline__ void xcd_barrier(const XcdBarrier& b, const bool xb_leader) {
;     asm volatile("s_waitcnt vmcnt(0)" ::: "memory");
;     __syncthreads();
;     if (xb_leader) {
;         unsigned* bar = b.bar;
;         __builtin_amdgcn_s_waitcnt(0);
;         unsigned nloc = b.st[0], nx = b.st[1];
;         if (nloc == 0u) { unsigned bal; xcd_barrier_complete(bar, b.x, nloc, nx, bal); b.st[0] = nloc; b.st[1] = nx; b.st[3] = bal; }
.LBB0_898:
	s_waitcnt vmcnt(0)
	s_waitcnt vmcnt(0) lgkmcnt(0)
	s_barrier
	s_and_saveexec_b64 s[0:1], s[6:7]
	s_cbranch_execz .LBB0_958
	s_add_i32 s3, 0, 0x20160
	v_mov_b32_e32 v0, s3
	s_waitcnt vmcnt(0) expcnt(0) lgkmcnt(0)
	buffer_inv sc1
	ds_read_b32 v9, v0
	s_add_i32 s3, 0, 0x20164
	v_mov_b32_e32 v0, s3
	ds_read_b32 v8, v0
	s_waitcnt lgkmcnt(1)
	v_cmp_ne_u32_e32 vcc, 0, v9
	s_cbranch_vccnz .LBB0_922
	v_readlane_b32 s6, v254, 0
	v_readlane_b32 s7, v254, 1
	s_load_dwordx2 s[10:11], s[6:7], 0x4
	s_add_u32 s6, s28, 0x1000
	s_addc_u32 s7, s29, 0
	s_add_u32 s8, s28, 0x1100
	s_addc_u32 s9, s29, 0
	s_waitcnt lgkmcnt(0)
	s_mul_i32 s3, s10, s33
	s_add_u32 s10, s28, 0x1200
	s_mul_i32 s3, s3, s11
	s_addc_u32 s11, s29, 0
	s_add_u32 s12, s28, 0x1300
	s_addc_u32 s13, s29, 0
	s_mov_b32 s42, 1
	v_mov_b32_e32 v8, 0
	s_branch .LBB0_903

; __device__ __forceinline__ void xcd_barrier(const XcdBarrier& b, const bool xb_leader) {
;     asm volatile("s_waitcnt vmcnt(0)" ::: "memory");
;     __syncthreads();
;     if (xb_leader) {
;         unsigned* bar = b.bar;
;         __builtin_amdgcn_s_waitcnt(0);
;         unsigned nloc = b.st[0], nx = b.st[1];
;         if (nloc == 0u) { unsigned bal; xcd_barrier_complete(bar, b.x, nloc, nx, bal); b.st[0] = nloc; b.st[1] = nx; b.st[3] = bal; }
.LBB0_1048:
	s_waitcnt vmcnt(0)
	s_waitcnt vmcnt(0) lgkmcnt(0)
	s_barrier
	s_and_saveexec_b64 s[0:1], s[4:5]
	s_cbranch_execz .LBB0_1108
	s_add_i32 s3, 0, 0x20160
	v_mov_b32_e32 v0, s3
	s_waitcnt vmcnt(0) expcnt(0) lgkmcnt(0)
	buffer_inv sc1
	ds_read_b32 v9, v0
	s_add_i32 s3, 0, 0x20164
	v_mov_b32_e32 v0, s3
	ds_read_b32 v8, v0
	s_waitcnt lgkmcnt(1)
	v_cmp_ne_u32_e32 vcc, 0, v9
	s_cbranch_vccnz .LBB0_1072
	v_readlane_b32 s4, v254, 0
	v_readlane_b32 s5, v254, 1
	s_load_dwordx2 s[8:9], s[4:5], 0x4
	s_add_u32 s4, s28, 0x1000
	s_addc_u32 s5, s29, 0
	s_add_u32 s6, s28, 0x1100
	s_addc_u32 s7, s29, 0
	s_waitcnt lgkmcnt(0)
	s_mul_i32 s3, s8, s33
	s_add_u32 s8, s28, 0x1200
	s_mul_i32 s3, s3, s9
	s_addc_u32 s9, s29, 0
	s_add_u32 s10, s28, 0x1300
	s_addc_u32 s11, s29, 0
	s_mov_b32 s42, 1
	v_mov_b32_e32 v8, 0
	s_branch .LBB0_1053

; __device__ __forceinline__ void xcd_barrier(const XcdBarrier& b, const bool xb_leader) {
;     asm volatile("s_waitcnt vmcnt(0)" ::: "memory");
;     __syncthreads();
;     if (xb_leader) {
;         unsigned* bar = b.bar;
;         __builtin_amdgcn_s_waitcnt(0);
;         unsigned nloc = b.st[0], nx = b.st[1];
;         if (nloc == 0u) { unsigned bal; xcd_barrier_complete(bar, b.x, nloc, nx, bal); b.st[0] = nloc; b.st[1] = nx; b.st[3] = bal; }
.LBB0_1188:
	s_waitcnt vmcnt(0)
	s_waitcnt vmcnt(0) lgkmcnt(0)
	s_barrier
	s_and_saveexec_b64 s[0:1], s[6:7]
	s_cbranch_execz .LBB0_1247
	s_add_i32 s3, 0, 0x20160
	v_mov_b32_e32 v0, s3
	s_waitcnt vmcnt(0) expcnt(0) lgkmcnt(0)
	buffer_inv sc1
	ds_read_b32 v9, v0
	s_add_i32 s3, 0, 0x20164
	v_mov_b32_e32 v0, s3
	ds_read_b32 v8, v0
	s_waitcnt lgkmcnt(1)
	v_cmp_ne_u32_e32 vcc, 0, v9
	s_cbranch_vccnz .LBB0_1211
	v_readlane_b32 s6, v254, 0
	v_readlane_b32 s7, v254, 1
	s_load_dwordx2 s[10:11], s[6:7], 0x4
	s_add_u32 s6, s28, 0x1000
	s_addc_u32 s7, s29, 0
	s_add_u32 s8, s28, 0x1100
	s_addc_u32 s9, s29, 0
	s_waitcnt lgkmcnt(0)
	s_mul_i32 s3, s10, s33
	s_add_u32 s10, s28, 0x1200
	s_mul_i32 s3, s3, s11
	s_addc_u32 s11, s29, 0
	s_add_u32 s12, s28, 0x1300
	s_addc_u32 s13, s29, 0
	s_mov_b32 s44, 1
	v_mov_b32_e32 v8, 0
	s_branch .LBB0_1193

; __device__ __forceinline__ unsigned xb_ld(unsigned* p)              { return __hip_atomic_load(p, __ATOMIC_RELAXED, __HIP_MEMORY_SCOPE_AGENT); }
; __device__ __forceinline__ unsigned xb_add(unsigned* p, unsigned v) { return __hip_atomic_fetch_add(p, v, __ATOMIC_RELAXED, __HIP_MEMORY_SCOPE_AGENT); }
; #define XB_SPIN(cond, bar) do { unsigned _sp = 0; while (cond) { __builtin_amdgcn_s_sleep(1); \
;     if ((++_sp & 255u) == 0u) { if (xb_ld(&(bar)[XB_TMO])) break; if (_sp > XB_SPIN_CAP) { atomicAdd(&(bar)[XB_TMO], 1u); break; } } } } while (0)
; __device__ __forceinline__ void xcc_barrier(unsigned* bar, unsigned* cnt, unsigned nloc, const bool xb_leader) {
;     asm volatile("s_waitcnt vmcnt(0)" ::: "memory");
;     __syncthreads();
;     if (xb_leader) {
;         __builtin_amdgcn_s_waitcnt(0);
;         const unsigned old = xb_add(cnt, 1u), target = (old / nloc + 1u) * nloc;
;         XB_SPIN(xb_ld(cnt) < target, bar);
.LBB0_1439:
	s_waitcnt vmcnt(0)
	s_waitcnt vmcnt(0) lgkmcnt(0)
	s_barrier
	s_and_saveexec_b64 s[4:5], s[6:7]
	s_cbranch_execz .LBB0_1455
	s_lshl_b32 s6, s82, 10
	s_ashr_i32 s7, s6, 31
	s_lshl_b64 s[6:7], s[6:7], 2
	s_add_u32 s3, s78, s6
	s_addc_u32 s6, s79, s7
	v_readlane_b32 s7, v254, 21
	s_lshl_b32 s7, s7, 8
	s_mov_b64 s[8:9], exec
	s_add_u32 s3, s3, s7
	s_addc_u32 s7, s6, 0
	v_mbcnt_lo_u32_b32 v0, s8, 0
	s_add_u32 s6, s3, 0xc000
	v_mbcnt_hi_u32_b32 v1, s9, v0
	s_addc_u32 s7, s7, 0
	v_cmp_eq_u32_e32 vcc, 0, v1
	s_waitcnt vmcnt(0) expcnt(0) lgkmcnt(0)
	buffer_inv sc1
	s_and_saveexec_b64 s[10:11], vcc
	s_cbranch_execz .LBB0_1442
	s_bcnt1_i32_b64 s3, s[8:9]
	v_mov_b32_e32 v0, 0
	v_mov_b32_e32 v2, s3
	global_atomic_add v2, v0, v2, s[6:7] sc0

; __device__ __forceinline__ void xcd_barrier(const XcdBarrier& b, const bool xb_leader) {
;     asm volatile("s_waitcnt vmcnt(0)" ::: "memory");
;     __syncthreads();
;     if (xb_leader) {
;         unsigned* bar = b.bar;
;         __builtin_amdgcn_s_waitcnt(0);
;         unsigned nloc = b.st[0], nx = b.st[1];
;         if (nloc == 0u) { unsigned bal; xcd_barrier_complete(bar, b.x, nloc, nx, bal); b.st[0] = nloc; b.st[1] = nx; b.st[3] = bal; }
.LBB0_1459:
	s_waitcnt vmcnt(0)
	s_waitcnt vmcnt(0) lgkmcnt(0)
	s_barrier
	s_and_saveexec_b64 s[4:5], s[6:7]
	s_cbranch_execz .LBB0_1519
	s_add_i32 s3, 0, 0x20160
	v_mov_b32_e32 v0, s3
	s_waitcnt vmcnt(0) expcnt(0) lgkmcnt(0)
	buffer_inv sc1
	ds_read_b32 v9, v0
	s_add_i32 s3, 0, 0x20164
	v_mov_b32_e32 v0, s3
	ds_read_b32 v8, v0
	s_waitcnt lgkmcnt(1)
	v_cmp_ne_u32_e32 vcc, 0, v9
	s_cbranch_vccnz .LBB0_1483
	v_readlane_b32 s6, v254, 0
	v_readlane_b32 s7, v254, 1
	s_load_dwordx2 s[10:11], s[6:7], 0x4
	s_add_u32 s6, s28, 0x1000
	s_addc_u32 s7, s29, 0
	s_add_u32 s8, s28, 0x1100
	s_addc_u32 s9, s29, 0
	s_waitcnt lgkmcnt(0)
	s_mul_i32 s3, s10, s33
	s_add_u32 s10, s28, 0x1200
	s_mul_i32 s3, s3, s11
	s_addc_u32 s11, s29, 0
	s_add_u32 s12, s28, 0x1300
	s_addc_u32 s13, s29, 0
	s_mov_b32 s42, 1
	v_mov_b32_e32 v8, 0
	s_branch .LBB0_1464

; __device__ __forceinline__ unsigned xb_ld(unsigned* p)              { return __hip_atomic_load(p, __ATOMIC_RELAXED, __HIP_MEMORY_SCOPE_AGENT); }
; __device__ __forceinline__ unsigned xb_add(unsigned* p, unsigned v) { return __hip_atomic_fetch_add(p, v, __ATOMIC_RELAXED, __HIP_MEMORY_SCOPE_AGENT); }
; #define XB_SPIN(cond, bar) do { unsigned _sp = 0; while (cond) { __builtin_amdgcn_s_sleep(1); \
;     if ((++_sp & 255u) == 0u) { if (xb_ld(&(bar)[XB_TMO])) break; if (_sp > XB_SPIN_CAP) { atomicAdd(&(bar)[XB_TMO], 1u); break; } } } } while (0)
; __device__ __forceinline__ void xcc_barrier(unsigned* bar, unsigned* cnt, unsigned nloc, const bool xb_leader) {
;     asm volatile("s_waitcnt vmcnt(0)" ::: "memory");
;     __syncthreads();
;     if (xb_leader) {
;         __builtin_amdgcn_s_waitcnt(0);
;         const unsigned old = xb_add(cnt, 1u), target = (old / nloc + 1u) * nloc;
;         XB_SPIN(xb_ld(cnt) < target, bar);
.LBB0_1546:
	s_waitcnt vmcnt(0)
	s_waitcnt vmcnt(0) lgkmcnt(0)
	s_barrier
	s_and_saveexec_b64 s[0:1], s[4:5]
	s_cbranch_execz .LBB0_1562
	s_lshl_b32 s4, s82, 10
	s_ashr_i32 s5, s4, 31
	s_lshl_b64 s[4:5], s[4:5], 2
	s_add_u32 s3, s78, s4
	s_addc_u32 s4, s79, s5
	v_readlane_b32 s5, v254, 21
	s_lshl_b32 s5, s5, 8
	s_mov_b64 s[6:7], exec
	s_add_u32 s3, s3, s5
	s_addc_u32 s5, s4, 0
	v_mbcnt_lo_u32_b32 v0, s6, 0
	s_add_u32 s4, s3, 0xc000
	v_mbcnt_hi_u32_b32 v1, s7, v0
	s_addc_u32 s5, s5, 0
	v_cmp_eq_u32_e32 vcc, 0, v1
	s_waitcnt vmcnt(0) expcnt(0) lgkmcnt(0)
	buffer_inv sc1
	s_and_saveexec_b64 s[10:11], vcc
	s_cbranch_execz .LBB0_1549
	s_bcnt1_i32_b64 s3, s[6:7]
	v_mov_b32_e32 v0, 0
	v_mov_b32_e32 v2, s3
	global_atomic_add v2, v0, v2, s[4:5] sc0

; __device__ __forceinline__ void xcd_barrier(const XcdBarrier& b, const bool xb_leader) {
;     asm volatile("s_waitcnt vmcnt(0)" ::: "memory");
;     __syncthreads();
;     if (xb_leader) {
;         unsigned* bar = b.bar;
;         __builtin_amdgcn_s_waitcnt(0);
;         unsigned nloc = b.st[0], nx = b.st[1];
;         if (nloc == 0u) { unsigned bal; xcd_barrier_complete(bar, b.x, nloc, nx, bal); b.st[0] = nloc; b.st[1] = nx; b.st[3] = bal; }
.LBB0_1566:
	s_waitcnt vmcnt(0)
	s_waitcnt vmcnt(0) lgkmcnt(0)
	s_barrier
	s_and_saveexec_b64 s[0:1], s[4:5]
	s_cbranch_execz .LBB0_1626
	s_add_i32 s3, 0, 0x20160
	v_mov_b32_e32 v0, s3
	s_waitcnt vmcnt(0) expcnt(0) lgkmcnt(0)
	buffer_inv sc1
	ds_read_b32 v9, v0
	s_add_i32 s3, 0, 0x20164
	v_mov_b32_e32 v0, s3
	ds_read_b32 v8, v0
	s_waitcnt lgkmcnt(1)
	v_cmp_ne_u32_e32 vcc, 0, v9
	s_cbranch_vccnz .LBB0_1590
	v_readlane_b32 s4, v254, 0
	v_readlane_b32 s5, v254, 1
	s_load_dwordx2 s[10:11], s[4:5], 0x4
	s_add_u32 s4, s28, 0x1000
	s_addc_u32 s5, s29, 0
	s_add_u32 s6, s28, 0x1100
	s_addc_u32 s7, s29, 0
	s_waitcnt lgkmcnt(0)
	s_mul_i32 s3, s10, s33
	s_add_u32 s10, s28, 0x1200
	s_mul_i32 s3, s3, s11
	s_addc_u32 s11, s29, 0
	s_add_u32 s12, s28, 0x1300
	s_addc_u32 s13, s29, 0
	s_mov_b32 s40, 1
	v_mov_b32_e32 v8, 0
	s_branch .LBB0_1571

; __device__ __forceinline__ unsigned xb_ld(unsigned* p)              { return __hip_atomic_load(p, __ATOMIC_RELAXED, __HIP_MEMORY_SCOPE_AGENT); }
; __device__ __forceinline__ unsigned xb_add(unsigned* p, unsigned v) { return __hip_atomic_fetch_add(p, v, __ATOMIC_RELAXED, __HIP_MEMORY_SCOPE_AGENT); }
; #define XB_SPIN(cond, bar) do { unsigned _sp = 0; while (cond) { __builtin_amdgcn_s_sleep(1); \
;     if ((++_sp & 255u) == 0u) { if (xb_ld(&(bar)[XB_TMO])) break; if (_sp > XB_SPIN_CAP) { atomicAdd(&(bar)[XB_TMO], 1u); break; } } } } while (0)
; __device__ __forceinline__ void xcd_barrier(const XcdBarrier& b, const bool xb_leader) {
;     ...
;             else XB_SPIN(xb_ld(&bar[XB_TOPGEN]) == tg, bar);
;             __builtin_amdgcn_fence(__ATOMIC_ACQUIRE, "agent");
;             xb_add(&bar[XB_XGEN(b.x)], 1u);
;             asm volatile("s_waitcnt vmcnt(0)" ::: "memory");
.LBB0_1623:
	s_or_b64 exec, exec, s[6:7]
	s_mov_b64 s[6:7], exec
	v_mbcnt_lo_u32_b32 v0, s6, 0
	v_mbcnt_hi_u32_b32 v0, s7, v0
	v_cmp_eq_u32_e32 vcc, 0, v0
	s_waitcnt vmcnt(0)
	s_and_saveexec_b64 s[10:11], vcc
	s_cbranch_execz .LBB0_1625
	s_bcnt1_i32_b64 s3, s[6:7]
	v_mov_b32_e32 v0, 0x2000
	v_mov_b32_e32 v1, s3
	global_atomic_add v0, v1, s[4:5] offset:1024

; __device__ __forceinline__ void xcd_barrier(const XcdBarrier& b, const bool xb_leader) {
;     asm volatile("s_waitcnt vmcnt(0)" ::: "memory");
;     __syncthreads();
;     if (xb_leader) {
;         unsigned* bar = b.bar;
;         __builtin_amdgcn_s_waitcnt(0);
;         unsigned nloc = b.st[0], nx = b.st[1];
;         if (nloc == 0u) { unsigned bal; xcd_barrier_complete(bar, b.x, nloc, nx, bal); b.st[0] = nloc; b.st[1] = nx; b.st[3] = bal; }
.LBB0_1771:
	s_waitcnt vmcnt(0)
	s_waitcnt vmcnt(0) lgkmcnt(0)
	s_barrier
	s_and_saveexec_b64 s[0:1], s[4:5]
	s_cbranch_execz .LBB0_1830
	s_add_i32 s3, 0, 0x20160
	v_mov_b32_e32 v0, s3
	s_waitcnt vmcnt(0) expcnt(0) lgkmcnt(0)
	buffer_inv sc1
	ds_read_b32 v9, v0
	s_add_i32 s3, 0, 0x20164
	v_mov_b32_e32 v0, s3
	ds_read_b32 v8, v0
	s_waitcnt lgkmcnt(1)
	v_cmp_ne_u32_e32 vcc, 0, v9
	s_cbranch_vccnz .LBB0_1794
	v_readlane_b32 s4, v254, 0
	v_readlane_b32 s5, v254, 1
	s_load_dwordx2 s[10:11], s[4:5], 0x4
	s_add_u32 s4, s28, 0x1000
	s_addc_u32 s5, s29, 0
	s_add_u32 s6, s28, 0x1100
	s_addc_u32 s7, s29, 0
	s_waitcnt lgkmcnt(0)
	s_mul_i32 s3, s10, s33
	s_add_u32 s10, s28, 0x1200
	s_mul_i32 s3, s3, s11
	s_addc_u32 s11, s29, 0
	s_add_u32 s12, s28, 0x1300
	s_addc_u32 s13, s29, 0
	s_mov_b32 s38, 1
	v_mov_b32_e32 v8, 0
	s_branch .LBB0_1776

; __device__ __forceinline__ void xcd_barrier(const XcdBarrier& b, const bool xb_leader) {
;     asm volatile("s_waitcnt vmcnt(0)" ::: "memory");
;     __syncthreads();
;     if (xb_leader) {
;         unsigned* bar = b.bar;
;         __builtin_amdgcn_s_waitcnt(0);
;         unsigned nloc = b.st[0], nx = b.st[1];
;         if (nloc == 0u) { unsigned bal; xcd_barrier_complete(bar, b.x, nloc, nx, bal); b.st[0] = nloc; b.st[1] = nx; b.st[3] = bal; }
.LBB0_1883:
	s_waitcnt vmcnt(0)
	s_waitcnt vmcnt(0) lgkmcnt(0)
	s_barrier
	s_and_saveexec_b64 s[6:7], s[0:1]
	s_cbranch_execz .LBB0_1942
	s_add_i32 s0, 0, 0x20160
	v_mov_b32_e32 v0, s0
	s_waitcnt vmcnt(0) expcnt(0) lgkmcnt(0)
	buffer_inv sc1
	ds_read_b32 v9, v0
	s_add_i32 s0, 0, 0x20164
	v_mov_b32_e32 v0, s0
	ds_read_b32 v8, v0
	s_waitcnt lgkmcnt(1)
	v_cmp_ne_u32_e32 vcc, 0, v9
	s_cbranch_vccnz .LBB0_1906
	v_readlane_b32 s0, v254, 0
	v_readlane_b32 s1, v254, 1
	s_load_dwordx2 s[8:9], s[0:1], 0x4
	s_add_u32 s0, s28, 0x1000
	s_addc_u32 s1, s29, 0
	s_add_u32 s2, s28, 0x1100
	s_addc_u32 s3, s29, 0
	s_waitcnt lgkmcnt(0)
	s_mul_i32 s24, s8, s33
	s_add_u32 s8, s28, 0x1200
	s_mul_i32 s24, s24, s9
	s_addc_u32 s9, s29, 0
	s_add_u32 s12, s28, 0x1300
	s_addc_u32 s13, s29, 0
	s_mov_b32 s37, 1
	v_mov_b32_e32 v8, 0
	s_branch .LBB0_1888

; __device__ __forceinline__ unsigned xb_ld(unsigned* p)              { return __hip_atomic_load(p, __ATOMIC_RELAXED, __HIP_MEMORY_SCOPE_AGENT); }
; __device__ __forceinline__ unsigned xb_add(unsigned* p, unsigned v) { return __hip_atomic_fetch_add(p, v, __ATOMIC_RELAXED, __HIP_MEMORY_SCOPE_AGENT); }
; #define XB_SPIN(cond, bar) do { unsigned _sp = 0; while (cond) { __builtin_amdgcn_s_sleep(1); \
;     if ((++_sp & 255u) == 0u) { if (xb_ld(&(bar)[XB_TMO])) break; if (_sp > XB_SPIN_CAP) { atomicAdd(&(bar)[XB_TMO], 1u); break; } } } } while (0)
; __device__ __forceinline__ void xcd_barrier(const XcdBarrier& b, const bool xb_leader) {
;     ...
;             else XB_SPIN(xb_ld(&bar[XB_TOPGEN]) == tg, bar);
;             __builtin_amdgcn_fence(__ATOMIC_ACQUIRE, "agent");
;             xb_add(&bar[XB_XGEN(b.x)], 1u);
;             asm volatile("s_waitcnt vmcnt(0)" ::: "memory");
.LBB0_1939:
	s_or_b64 exec, exec, s[2:3]
	s_mov_b64 s[2:3], exec
	v_mbcnt_lo_u32_b32 v0, s2, 0
	v_mbcnt_hi_u32_b32 v0, s3, v0
	v_cmp_eq_u32_e32 vcc, 0, v0
	s_waitcnt vmcnt(0)
	s_and_saveexec_b64 s[8:9], vcc
	s_cbranch_execz .LBB0_1941
	s_bcnt1_i32_b64 s2, s[2:3]
	v_mov_b32_e32 v0, 0x2000
	v_mov_b32_e32 v1, s2
	global_atomic_add v0, v1, s[0:1] offset:1024
